# grid barrier: all waiters poll the cross-XCD arrival counter (signed compare against the round total) instead of release generations; saves polling hops per barrier
# speedup vs baseline: 1.0101x; 1.0051x over previous
; __device__ __forceinline__ unsigned xb_ld(unsigned* p)              { return __hip_atomic_load(p, __ATOMIC_RELAXED, __HIP_MEMORY_SCOPE_AGENT); }
; __device__ __forceinline__ unsigned xb_add(unsigned* p, unsigned v) { return __hip_atomic_fetch_add(p, v, __ATOMIC_RELAXED, __HIP_MEMORY_SCOPE_AGENT); }
; #define XB_SPIN(cond, bar) do { unsigned _sp = 0; while (cond) { __builtin_amdgcn_s_sleep(1); \
;     if ((++_sp & 255u) == 0u) { if (xb_ld(&(bar)[XB_TMO])) break; if (_sp > XB_SPIN_CAP) { atomicAdd(&(bar)[XB_TMO], 1u); break; } } } } while (0)
; __device__ __forceinline__ void xcd_barrier(const XcdBarrier& b) {
;     ...
;         const unsigned old = xb_add(&bar[XB_XSUB(b.x)], 1u);
;         const unsigned gen = old / nloc;
;         if (old + 1u == (gen + 1u) * nloc) {
;             __builtin_amdgcn_fence(__ATOMIC_RELEASE, "agent");
;             asm volatile("s_waitcnt vmcnt(0)" ::: "memory");
;             const unsigned og = xb_add(&bar[XB_TOP], 1u);
;             const unsigned tg = og / nx;
;             if (og + 1u == (tg + 1u) * nx) xb_add(&bar[XB_TOPGEN], 1u);
;             else XB_SPIN(xb_ld(&bar[XB_TOPGEN]) == tg, bar);
;             __builtin_amdgcn_fence(__ATOMIC_ACQUIRE, "agent");
;             xb_add(&bar[XB_XGEN(b.x)], 1u);
;             asm volatile("s_waitcnt vmcnt(0)" ::: "memory");
;         } else {
;             XB_SPIN(xb_ld(&bar[XB_XGEN(b.x)]) == gen, bar);
.LBB0_329:
	s_or_b64 exec, exec, s[8:9]
	v_cvt_f32_u32_e32 v4, v2
	s_waitcnt vmcnt(0)
	v_readfirstlane_b32 s6, v3
	v_sub_u32_e32 v3, 0, v2
	v_rcp_iflag_f32_e32 v4, v4
	v_add_u32_e32 v5, s6, v1
	v_mul_f32_e32 v4, 0x4f7ffffe, v4
	v_cvt_u32_f32_e32 v4, v4
	v_mul_lo_u32 v1, v3, v4
	v_mul_hi_u32 v1, v4, v1
	v_add_u32_e32 v1, v4, v1
	v_mul_hi_u32 v1, v5, v1
	v_mul_lo_u32 v3, v1, v2
	v_sub_u32_e32 v3, v5, v3
	v_add_u32_e32 v4, 1, v1
	v_cmp_ge_u32_e32 vcc, v3, v2
	s_nop 1
	v_cndmask_b32_e32 v1, v1, v4, vcc
	v_sub_u32_e32 v4, v3, v2
	v_cndmask_b32_e32 v3, v3, v4, vcc
	v_add_u32_e32 v4, 1, v1
	v_cmp_ge_u32_e32 vcc, v3, v2
	v_add_u32_e32 v3, 1, v5
	s_nop 0
	v_cndmask_b32_e32 v1, v1, v4, vcc
	v_mul_lo_u32 v4, v2, v1
	v_add_u32_e32 v2, v4, v2
	v_cmp_ne_u32_e32 vcc, v3, v2
	s_and_saveexec_b64 s[6:7], vcc
	s_xor_b64 s[6:7], exec, s[6:7]
	s_cbranch_execz .LBB0_343
	s_waitcnt lgkmcnt(0)
	s_add_u32 s12, s78, 0x7400
	s_addc_u32 s13, s79, 0
	v_mad_u32_u24 v1, v1, v0, v0
	v_mov_b32_e32 v0, 0
	global_load_dword v0, v0, s[12:13] sc1
	s_waitcnt vmcnt(0)
	v_sub_u32_e32 v0, v0, v1
	v_cmp_gt_i32_e32 vcc, 0, v0
	s_and_saveexec_b64 s[8:9], vcc
	s_cbranch_execz .LBB0_342
	s_add_u32 s10, s78, 0x4200
	s_addc_u32 s11, s79, 0
	s_mov_b32 s24, 1
	s_mov_b64 s[14:15], 0
	v_mov_b32_e32 v0, 0
	s_branch .LBB0_333

; __device__ __forceinline__ unsigned xb_ld(unsigned* p)              { return __hip_atomic_load(p, __ATOMIC_RELAXED, __HIP_MEMORY_SCOPE_AGENT); }
; #define XB_SPIN(cond, bar) do { unsigned _sp = 0; while (cond) { __builtin_amdgcn_s_sleep(1); \
;     if ((++_sp & 255u) == 0u) { if (xb_ld(&(bar)[XB_TMO])) break; if (_sp > XB_SPIN_CAP) { atomicAdd(&(bar)[XB_TMO], 1u); break; } } } } while (0)
; __device__ __forceinline__ void xcd_barrier(const XcdBarrier& b) {
;     ...
;             XB_SPIN(xb_ld(&bar[XB_XGEN(b.x)]) == gen, bar);
.LBB0_335:
	global_load_dword v2, v0, s[12:13] sc1
	s_add_i32 s24, s24, 1
	s_mov_b64 s[20:21], -1
	s_waitcnt vmcnt(0)
	v_sub_u32_e32 v2, v2, v1
	v_cmp_le_i32_e32 vcc, 0, v2
	s_orn2_b64 s[18:19], vcc, exec
	s_branch .LBB0_332

; __device__ __forceinline__ unsigned xb_ld(unsigned* p)              { return __hip_atomic_load(p, __ATOMIC_RELAXED, __HIP_MEMORY_SCOPE_AGENT); }
; __device__ __forceinline__ unsigned xb_add(unsigned* p, unsigned v) { return __hip_atomic_fetch_add(p, v, __ATOMIC_RELAXED, __HIP_MEMORY_SCOPE_AGENT); }
; #define XB_SPIN(cond, bar) do { unsigned _sp = 0; while (cond) { __builtin_amdgcn_s_sleep(1); \
;     if ((++_sp & 255u) == 0u) { if (xb_ld(&(bar)[XB_TMO])) break; if (_sp > XB_SPIN_CAP) { atomicAdd(&(bar)[XB_TMO], 1u); break; } } } } while (0)
; __device__ __forceinline__ void xcd_barrier(const XcdBarrier& b) {
;     ...
;         if (old + 1u == (gen + 1u) * nloc) {
;             __builtin_amdgcn_fence(__ATOMIC_RELEASE, "agent");
;             asm volatile("s_waitcnt vmcnt(0)" ::: "memory");
;             const unsigned og = xb_add(&bar[XB_TOP], 1u);
;             const unsigned tg = og / nx;
;             if (og + 1u == (tg + 1u) * nx) xb_add(&bar[XB_TOPGEN], 1u);
;             else XB_SPIN(xb_ld(&bar[XB_TOPGEN]) == tg, bar);
.LBB0_346:
	s_or_b64 exec, exec, s[8:9]
	v_cvt_f32_u32_e32 v3, v0
	s_waitcnt vmcnt(0)
	v_readfirstlane_b32 s6, v2
	s_add_u32 s8, s78, 0x7500
	s_addc_u32 s9, s79, 0
	v_rcp_iflag_f32_e32 v3, v3
	v_add_u32_e32 v1, s6, v1
	v_add_u32_e32 v4, 1, v1
	s_mov_b64 s[10:11], -1
	v_mul_f32_e32 v2, 0x4f7ffffe, v3
	v_cvt_u32_f32_e32 v2, v2
	v_sub_u32_e32 v3, 0, v0
	v_mul_lo_u32 v3, v3, v2
	v_mul_hi_u32 v3, v2, v3
	v_add_u32_e32 v2, v2, v3
	v_mul_hi_u32 v2, v1, v2
	v_mul_lo_u32 v3, v2, v0
	v_sub_u32_e32 v1, v1, v3
	v_add_u32_e32 v5, 1, v2
	v_cmp_ge_u32_e32 vcc, v1, v0
	v_sub_u32_e32 v3, v1, v0
	s_nop 0
	v_cndmask_b32_e32 v2, v2, v5, vcc
	v_cndmask_b32_e32 v1, v1, v3, vcc
	v_add_u32_e32 v3, 1, v2
	v_cmp_ge_u32_e32 vcc, v1, v0
	s_nop 1
	v_cndmask_b32_e32 v2, v2, v3, vcc
	v_mul_lo_u32 v1, v0, v2
	v_add_u32_e32 v0, v1, v0
	v_mov_b32_e32 v6, v0
	v_cmp_ne_u32_e32 vcc, v4, v0
	v_mov_b64_e32 v[0:1], s[8:9]
	s_and_saveexec_b64 s[6:7], vcc
	s_cbranch_execz .LBB0_358
	s_sub_u32 s8, s8, 0x100
	s_subb_u32 s9, s9, 0
	v_mov_b32_e32 v0, 0
	global_load_dword v1, v0, s[8:9] sc1
	s_mov_b64 s[14:15], 0
	s_waitcnt vmcnt(0)
	v_sub_u32_e32 v1, v1, v6
	v_cmp_gt_i32_e32 vcc, 0, v1
	s_and_saveexec_b64 s[12:13], vcc
	s_cbranch_execz .LBB0_357
	s_add_u32 s10, s78, 0x4200
	s_addc_u32 s11, s79, 0
	s_mov_b32 s24, 1
	s_branch .LBB0_350

; __device__ __forceinline__ unsigned xb_ld(unsigned* p)              { return __hip_atomic_load(p, __ATOMIC_RELAXED, __HIP_MEMORY_SCOPE_AGENT); }
; #define XB_SPIN(cond, bar) do { unsigned _sp = 0; while (cond) { __builtin_amdgcn_s_sleep(1); \
;     if ((++_sp & 255u) == 0u) { if (xb_ld(&(bar)[XB_TMO])) break; if (_sp > XB_SPIN_CAP) { atomicAdd(&(bar)[XB_TMO], 1u); break; } } } } while (0)
; __device__ __forceinline__ void xcd_barrier(const XcdBarrier& b) {
;     ...
;             else XB_SPIN(xb_ld(&bar[XB_TOPGEN]) == tg, bar);
.LBB0_352:
	global_load_dword v1, v0, s[8:9] sc1
	s_add_i32 s24, s24, 1
	s_mov_b64 s[18:19], -1
	s_waitcnt vmcnt(0)
	v_sub_u32_e32 v1, v1, v6
	v_cmp_le_i32_e32 vcc, 0, v1
	s_orn2_b64 s[22:23], vcc, exec
	s_branch .LBB0_349

; __device__ __forceinline__ unsigned xb_ld(unsigned* p)              { return __hip_atomic_load(p, __ATOMIC_RELAXED, __HIP_MEMORY_SCOPE_AGENT); }
; __device__ __forceinline__ unsigned xb_add(unsigned* p, unsigned v) { return __hip_atomic_fetch_add(p, v, __ATOMIC_RELAXED, __HIP_MEMORY_SCOPE_AGENT); }
; #define XB_SPIN(cond, bar) do { unsigned _sp = 0; while (cond) { __builtin_amdgcn_s_sleep(1); \
;     if ((++_sp & 255u) == 0u) { if (xb_ld(&(bar)[XB_TMO])) break; if (_sp > XB_SPIN_CAP) { atomicAdd(&(bar)[XB_TMO], 1u); break; } } } } while (0)
; __device__ __forceinline__ void xcd_barrier(const XcdBarrier& b) {
;     ...
;         const unsigned old = xb_add(&bar[XB_XSUB(b.x)], 1u);
;         const unsigned gen = old / nloc;
;         if (old + 1u == (gen + 1u) * nloc) {
;             __builtin_amdgcn_fence(__ATOMIC_RELEASE, "agent");
;             asm volatile("s_waitcnt vmcnt(0)" ::: "memory");
;             const unsigned og = xb_add(&bar[XB_TOP], 1u);
;             const unsigned tg = og / nx;
;             if (og + 1u == (tg + 1u) * nx) xb_add(&bar[XB_TOPGEN], 1u);
;             else XB_SPIN(xb_ld(&bar[XB_TOPGEN]) == tg, bar);
;             __builtin_amdgcn_fence(__ATOMIC_ACQUIRE, "agent");
;             xb_add(&bar[XB_XGEN(b.x)], 1u);
;             asm volatile("s_waitcnt vmcnt(0)" ::: "memory");
;         } else {
;             XB_SPIN(xb_ld(&bar[XB_XGEN(b.x)]) == gen, bar);
.LBB0_472:
	s_or_b64 exec, exec, s[6:7]
	v_cvt_f32_u32_e32 v4, v2
	s_waitcnt vmcnt(0)
	v_readfirstlane_b32 s4, v3
	v_sub_u32_e32 v3, 0, v2
	v_rcp_iflag_f32_e32 v4, v4
	v_add_u32_e32 v5, s4, v1
	v_mul_f32_e32 v4, 0x4f7ffffe, v4
	v_cvt_u32_f32_e32 v4, v4
	v_mul_lo_u32 v1, v3, v4
	v_mul_hi_u32 v1, v4, v1
	v_add_u32_e32 v1, v4, v1
	v_mul_hi_u32 v1, v5, v1
	v_mul_lo_u32 v3, v1, v2
	v_sub_u32_e32 v3, v5, v3
	v_add_u32_e32 v4, 1, v1
	v_cmp_ge_u32_e32 vcc, v3, v2
	s_nop 1
	v_cndmask_b32_e32 v1, v1, v4, vcc
	v_sub_u32_e32 v4, v3, v2
	v_cndmask_b32_e32 v3, v3, v4, vcc
	v_add_u32_e32 v4, 1, v1
	v_cmp_ge_u32_e32 vcc, v3, v2
	v_add_u32_e32 v3, 1, v5
	s_nop 0
	v_cndmask_b32_e32 v1, v1, v4, vcc
	v_mul_lo_u32 v4, v2, v1
	v_add_u32_e32 v2, v4, v2
	v_cmp_ne_u32_e32 vcc, v3, v2
	s_and_saveexec_b64 s[4:5], vcc
	s_xor_b64 s[4:5], exec, s[4:5]
	s_cbranch_execz .LBB0_486
	s_waitcnt lgkmcnt(0)
	s_add_u32 s10, s78, 0x7400
	s_addc_u32 s11, s79, 0
	v_mad_u32_u24 v1, v1, v0, v0
	v_mov_b32_e32 v0, 0
	global_load_dword v0, v0, s[10:11] sc1
	s_waitcnt vmcnt(0)
	v_sub_u32_e32 v0, v0, v1
	v_cmp_gt_i32_e32 vcc, 0, v0
	s_and_saveexec_b64 s[6:7], vcc
	s_cbranch_execz .LBB0_485
	s_add_u32 s8, s78, 0x4200
	s_addc_u32 s9, s79, 0
	s_mov_b32 s22, 1
	s_mov_b64 s[12:13], 0
	v_mov_b32_e32 v0, 0
	s_branch .LBB0_476

; __device__ __forceinline__ unsigned xb_ld(unsigned* p)              { return __hip_atomic_load(p, __ATOMIC_RELAXED, __HIP_MEMORY_SCOPE_AGENT); }
; #define XB_SPIN(cond, bar) do { unsigned _sp = 0; while (cond) { __builtin_amdgcn_s_sleep(1); \
;     if ((++_sp & 255u) == 0u) { if (xb_ld(&(bar)[XB_TMO])) break; if (_sp > XB_SPIN_CAP) { atomicAdd(&(bar)[XB_TMO], 1u); break; } } } } while (0)
; __device__ __forceinline__ void xcd_barrier(const XcdBarrier& b) {
;     ...
;             XB_SPIN(xb_ld(&bar[XB_XGEN(b.x)]) == gen, bar);
.LBB0_478:
	global_load_dword v2, v0, s[10:11] sc1
	s_add_i32 s22, s22, 1
	s_mov_b64 s[18:19], -1
	s_waitcnt vmcnt(0)
	v_sub_u32_e32 v2, v2, v1
	v_cmp_le_i32_e32 vcc, 0, v2
	s_orn2_b64 s[16:17], vcc, exec
	s_branch .LBB0_475

; __device__ __forceinline__ unsigned xb_ld(unsigned* p)              { return __hip_atomic_load(p, __ATOMIC_RELAXED, __HIP_MEMORY_SCOPE_AGENT); }
; __device__ __forceinline__ unsigned xb_add(unsigned* p, unsigned v) { return __hip_atomic_fetch_add(p, v, __ATOMIC_RELAXED, __HIP_MEMORY_SCOPE_AGENT); }
; #define XB_SPIN(cond, bar) do { unsigned _sp = 0; while (cond) { __builtin_amdgcn_s_sleep(1); \
;     if ((++_sp & 255u) == 0u) { if (xb_ld(&(bar)[XB_TMO])) break; if (_sp > XB_SPIN_CAP) { atomicAdd(&(bar)[XB_TMO], 1u); break; } } } } while (0)
; __device__ __forceinline__ void xcd_barrier(const XcdBarrier& b) {
;     ...
;         if (old + 1u == (gen + 1u) * nloc) {
;             __builtin_amdgcn_fence(__ATOMIC_RELEASE, "agent");
;             asm volatile("s_waitcnt vmcnt(0)" ::: "memory");
;             const unsigned og = xb_add(&bar[XB_TOP], 1u);
;             const unsigned tg = og / nx;
;             if (og + 1u == (tg + 1u) * nx) xb_add(&bar[XB_TOPGEN], 1u);
;             else XB_SPIN(xb_ld(&bar[XB_TOPGEN]) == tg, bar);
.LBB0_489:
	s_or_b64 exec, exec, s[6:7]
	v_cvt_f32_u32_e32 v3, v0
	s_waitcnt vmcnt(0)
	v_readfirstlane_b32 s4, v2
	s_add_u32 s6, s78, 0x7500
	s_addc_u32 s7, s79, 0
	v_rcp_iflag_f32_e32 v3, v3
	v_add_u32_e32 v1, s4, v1
	v_add_u32_e32 v4, 1, v1
	s_mov_b64 s[8:9], -1
	v_mul_f32_e32 v2, 0x4f7ffffe, v3
	v_cvt_u32_f32_e32 v2, v2
	v_sub_u32_e32 v3, 0, v0
	v_mul_lo_u32 v3, v3, v2
	v_mul_hi_u32 v3, v2, v3
	v_add_u32_e32 v2, v2, v3
	v_mul_hi_u32 v2, v1, v2
	v_mul_lo_u32 v3, v2, v0
	v_sub_u32_e32 v1, v1, v3
	v_add_u32_e32 v5, 1, v2
	v_cmp_ge_u32_e32 vcc, v1, v0
	v_sub_u32_e32 v3, v1, v0
	s_nop 0
	v_cndmask_b32_e32 v2, v2, v5, vcc
	v_cndmask_b32_e32 v1, v1, v3, vcc
	v_add_u32_e32 v3, 1, v2
	v_cmp_ge_u32_e32 vcc, v1, v0
	s_nop 1
	v_cndmask_b32_e32 v2, v2, v3, vcc
	v_mul_lo_u32 v1, v0, v2
	v_add_u32_e32 v0, v1, v0
	v_mov_b32_e32 v6, v0
	v_cmp_ne_u32_e32 vcc, v4, v0
	v_mov_b64_e32 v[0:1], s[6:7]
	s_and_saveexec_b64 s[4:5], vcc
	s_cbranch_execz .LBB0_501
	s_sub_u32 s6, s6, 0x100
	s_subb_u32 s7, s7, 0
	v_mov_b32_e32 v0, 0
	global_load_dword v1, v0, s[6:7] sc1
	s_mov_b64 s[12:13], 0
	s_waitcnt vmcnt(0)
	v_sub_u32_e32 v1, v1, v6
	v_cmp_gt_i32_e32 vcc, 0, v1
	s_and_saveexec_b64 s[10:11], vcc
	s_cbranch_execz .LBB0_500
	s_add_u32 s8, s78, 0x4200
	s_addc_u32 s9, s79, 0
	s_mov_b32 s22, 1
	s_branch .LBB0_493

; __device__ __forceinline__ unsigned xb_ld(unsigned* p)              { return __hip_atomic_load(p, __ATOMIC_RELAXED, __HIP_MEMORY_SCOPE_AGENT); }
; #define XB_SPIN(cond, bar) do { unsigned _sp = 0; while (cond) { __builtin_amdgcn_s_sleep(1); \
;     if ((++_sp & 255u) == 0u) { if (xb_ld(&(bar)[XB_TMO])) break; if (_sp > XB_SPIN_CAP) { atomicAdd(&(bar)[XB_TMO], 1u); break; } } } } while (0)
; __device__ __forceinline__ void xcd_barrier(const XcdBarrier& b) {
;     ...
;             else XB_SPIN(xb_ld(&bar[XB_TOPGEN]) == tg, bar);
.LBB0_495:
	global_load_dword v1, v0, s[6:7] sc1
	s_add_i32 s22, s22, 1
	s_mov_b64 s[16:17], -1
	s_waitcnt vmcnt(0)
	v_sub_u32_e32 v1, v1, v6
	v_cmp_le_i32_e32 vcc, 0, v1
	s_orn2_b64 s[20:21], vcc, exec
	s_branch .LBB0_492

; __device__ __forceinline__ unsigned xb_ld(unsigned* p)              { return __hip_atomic_load(p, __ATOMIC_RELAXED, __HIP_MEMORY_SCOPE_AGENT); }
; __device__ __forceinline__ unsigned xb_add(unsigned* p, unsigned v) { return __hip_atomic_fetch_add(p, v, __ATOMIC_RELAXED, __HIP_MEMORY_SCOPE_AGENT); }
; #define XB_SPIN(cond, bar) do { unsigned _sp = 0; while (cond) { __builtin_amdgcn_s_sleep(1); \
;     if ((++_sp & 255u) == 0u) { if (xb_ld(&(bar)[XB_TMO])) break; if (_sp > XB_SPIN_CAP) { atomicAdd(&(bar)[XB_TMO], 1u); break; } } } } while (0)
; __device__ __forceinline__ void xcd_barrier(const XcdBarrier& b) {
;     ...
;         const unsigned old = xb_add(&bar[XB_XSUB(b.x)], 1u);
;         const unsigned gen = old / nloc;
;         if (old + 1u == (gen + 1u) * nloc) {
;             __builtin_amdgcn_fence(__ATOMIC_RELEASE, "agent");
;             asm volatile("s_waitcnt vmcnt(0)" ::: "memory");
;             const unsigned og = xb_add(&bar[XB_TOP], 1u);
;             const unsigned tg = og / nx;
;             if (og + 1u == (tg + 1u) * nx) xb_add(&bar[XB_TOPGEN], 1u);
;             else XB_SPIN(xb_ld(&bar[XB_TOPGEN]) == tg, bar);
;             __builtin_amdgcn_fence(__ATOMIC_ACQUIRE, "agent");
;             xb_add(&bar[XB_XGEN(b.x)], 1u);
;             asm volatile("s_waitcnt vmcnt(0)" ::: "memory");
;         } else {
;             XB_SPIN(xb_ld(&bar[XB_XGEN(b.x)]) == gen, bar);
.LBB0_705:
	s_or_b64 exec, exec, s[10:11]
	v_cvt_f32_u32_e32 v4, v2
	s_waitcnt vmcnt(0)
	v_readfirstlane_b32 s8, v3
	v_sub_u32_e32 v3, 0, v2
	v_rcp_iflag_f32_e32 v4, v4
	v_add_u32_e32 v5, s8, v1
	v_mul_f32_e32 v4, 0x4f7ffffe, v4
	v_cvt_u32_f32_e32 v4, v4
	v_mul_lo_u32 v1, v3, v4
	v_mul_hi_u32 v1, v4, v1
	v_add_u32_e32 v1, v4, v1
	v_mul_hi_u32 v1, v5, v1
	v_mul_lo_u32 v3, v1, v2
	v_sub_u32_e32 v3, v5, v3
	v_add_u32_e32 v4, 1, v1
	v_cmp_ge_u32_e32 vcc, v3, v2
	s_nop 1
	v_cndmask_b32_e32 v1, v1, v4, vcc
	v_sub_u32_e32 v4, v3, v2
	v_cndmask_b32_e32 v3, v3, v4, vcc
	v_add_u32_e32 v4, 1, v1
	v_cmp_ge_u32_e32 vcc, v3, v2
	v_add_u32_e32 v3, 1, v5
	s_nop 0
	v_cndmask_b32_e32 v1, v1, v4, vcc
	v_mul_lo_u32 v4, v2, v1
	v_add_u32_e32 v2, v4, v2
	v_cmp_ne_u32_e32 vcc, v3, v2
	s_and_saveexec_b64 s[8:9], vcc
	s_xor_b64 s[8:9], exec, s[8:9]
	s_cbranch_execz .LBB0_719
	s_waitcnt lgkmcnt(0)
	s_add_u32 s14, s78, 0x7400
	s_addc_u32 s15, s79, 0
	v_mad_u32_u24 v1, v1, v0, v0
	v_mov_b32_e32 v0, 0
	global_load_dword v0, v0, s[14:15] sc1
	s_waitcnt vmcnt(0)
	v_sub_u32_e32 v0, v0, v1
	v_cmp_gt_i32_e32 vcc, 0, v0
	s_and_saveexec_b64 s[10:11], vcc
	s_cbranch_execz .LBB0_718
	s_add_u32 s12, s78, 0x4200
	s_addc_u32 s13, s79, 0
	s_mov_b32 s26, 1
	s_mov_b64 s[16:17], 0
	v_mov_b32_e32 v0, 0
	s_branch .LBB0_709

; __device__ __forceinline__ unsigned xb_ld(unsigned* p)              { return __hip_atomic_load(p, __ATOMIC_RELAXED, __HIP_MEMORY_SCOPE_AGENT); }
; #define XB_SPIN(cond, bar) do { unsigned _sp = 0; while (cond) { __builtin_amdgcn_s_sleep(1); \
;     if ((++_sp & 255u) == 0u) { if (xb_ld(&(bar)[XB_TMO])) break; if (_sp > XB_SPIN_CAP) { atomicAdd(&(bar)[XB_TMO], 1u); break; } } } } while (0)
; __device__ __forceinline__ void xcd_barrier(const XcdBarrier& b) {
;     ...
;             XB_SPIN(xb_ld(&bar[XB_XGEN(b.x)]) == gen, bar);
.LBB0_711:
	global_load_dword v2, v0, s[14:15] sc1
	s_add_i32 s26, s26, 1
	s_mov_b64 s[22:23], -1
	s_waitcnt vmcnt(0)
	v_sub_u32_e32 v2, v2, v1
	v_cmp_le_i32_e32 vcc, 0, v2
	s_orn2_b64 s[20:21], vcc, exec
	s_branch .LBB0_708

; __device__ __forceinline__ unsigned xb_ld(unsigned* p)              { return __hip_atomic_load(p, __ATOMIC_RELAXED, __HIP_MEMORY_SCOPE_AGENT); }
; __device__ __forceinline__ unsigned xb_add(unsigned* p, unsigned v) { return __hip_atomic_fetch_add(p, v, __ATOMIC_RELAXED, __HIP_MEMORY_SCOPE_AGENT); }
; #define XB_SPIN(cond, bar) do { unsigned _sp = 0; while (cond) { __builtin_amdgcn_s_sleep(1); \
;     if ((++_sp & 255u) == 0u) { if (xb_ld(&(bar)[XB_TMO])) break; if (_sp > XB_SPIN_CAP) { atomicAdd(&(bar)[XB_TMO], 1u); break; } } } } while (0)
; __device__ __forceinline__ void xcd_barrier(const XcdBarrier& b) {
;     ...
;             asm volatile("s_waitcnt vmcnt(0)" ::: "memory");
;             const unsigned og = xb_add(&bar[XB_TOP], 1u);
;             const unsigned tg = og / nx;
;             if (og + 1u == (tg + 1u) * nx) xb_add(&bar[XB_TOPGEN], 1u);
;             else XB_SPIN(xb_ld(&bar[XB_TOPGEN]) == tg, bar);
.LBB0_722:
	s_or_b64 exec, exec, s[10:11]
	v_cvt_f32_u32_e32 v3, v0
	s_waitcnt vmcnt(0)
	v_readfirstlane_b32 s8, v2
	s_add_u32 s10, s78, 0x7500
	s_addc_u32 s11, s79, 0
	v_rcp_iflag_f32_e32 v3, v3
	v_add_u32_e32 v1, s8, v1
	v_add_u32_e32 v4, 1, v1
	s_mov_b64 s[12:13], -1
	v_mul_f32_e32 v2, 0x4f7ffffe, v3
	v_cvt_u32_f32_e32 v2, v2
	v_sub_u32_e32 v3, 0, v0
	v_mul_lo_u32 v3, v3, v2
	v_mul_hi_u32 v3, v2, v3
	v_add_u32_e32 v2, v2, v3
	v_mul_hi_u32 v2, v1, v2
	v_mul_lo_u32 v3, v2, v0
	v_sub_u32_e32 v1, v1, v3
	v_add_u32_e32 v5, 1, v2
	v_cmp_ge_u32_e32 vcc, v1, v0
	v_sub_u32_e32 v3, v1, v0
	s_nop 0
	v_cndmask_b32_e32 v2, v2, v5, vcc
	v_cndmask_b32_e32 v1, v1, v3, vcc
	v_add_u32_e32 v3, 1, v2
	v_cmp_ge_u32_e32 vcc, v1, v0
	s_nop 1
	v_cndmask_b32_e32 v2, v2, v3, vcc
	v_mul_lo_u32 v1, v0, v2
	v_add_u32_e32 v0, v1, v0
	v_mov_b32_e32 v6, v0
	v_cmp_ne_u32_e32 vcc, v4, v0
	v_mov_b64_e32 v[0:1], s[10:11]
	s_and_saveexec_b64 s[8:9], vcc
	s_cbranch_execz .LBB0_734
	s_sub_u32 s10, s10, 0x100
	s_subb_u32 s11, s11, 0
	v_mov_b32_e32 v0, 0
	global_load_dword v1, v0, s[10:11] sc1
	s_mov_b64 s[16:17], 0
	s_waitcnt vmcnt(0)
	v_sub_u32_e32 v1, v1, v6
	v_cmp_gt_i32_e32 vcc, 0, v1
	s_and_saveexec_b64 s[14:15], vcc
	s_cbranch_execz .LBB0_733
	s_add_u32 s12, s78, 0x4200
	s_addc_u32 s13, s79, 0
	s_mov_b32 s26, 1
	s_branch .LBB0_726

; __device__ __forceinline__ unsigned xb_ld(unsigned* p)              { return __hip_atomic_load(p, __ATOMIC_RELAXED, __HIP_MEMORY_SCOPE_AGENT); }
; #define XB_SPIN(cond, bar) do { unsigned _sp = 0; while (cond) { __builtin_amdgcn_s_sleep(1); \
;     if ((++_sp & 255u) == 0u) { if (xb_ld(&(bar)[XB_TMO])) break; if (_sp > XB_SPIN_CAP) { atomicAdd(&(bar)[XB_TMO], 1u); break; } } } } while (0)
; __device__ __forceinline__ void xcd_barrier(const XcdBarrier& b) {
;     ...
;             else XB_SPIN(xb_ld(&bar[XB_TOPGEN]) == tg, bar);
.LBB0_728:
	global_load_dword v1, v0, s[10:11] sc1
	s_add_i32 s26, s26, 1
	s_mov_b64 s[20:21], -1
	s_waitcnt vmcnt(0)
	v_sub_u32_e32 v1, v1, v6
	v_cmp_le_i32_e32 vcc, 0, v1
	s_orn2_b64 s[24:25], vcc, exec
	s_branch .LBB0_725
